# gemm1: nt hint on the f32 output stores (never re-read on the device)
# speedup vs baseline: 1.0114x; 1.0025x over previous
.Lus_g1_a:
	s_mov_b64 vcc, s[0:1]
	s_waitcnt vmcnt(0)
	v_pk_add_f32 v[118:119], v[142:143], v[118:119]
	v_pk_add_f32 v[116:117], v[140:141], v[116:117]
	v_pk_add_f32 v[126:127], v[138:139], v[126:127]
	v_pk_add_f32 v[50:51], v[130:131], v[50:51]
	v_pk_add_f32 v[48:49], v[128:129], v[48:49]
	v_pk_add_f32 v[124:125], v[136:137], v[124:125]
	v_pk_add_f32 v[122:123], v[134:135], v[122:123]
	v_pk_add_f32 v[120:121], v[132:133], v[120:121]
	v_pk_add_f32 v[114:115], v[130:131], v[114:115]
	v_pk_add_f32 v[112:113], v[128:129], v[112:113]
	v_pk_add_f32 v[110:111], v[142:143], v[110:111]
	v_pk_add_f32 v[108:109], v[140:141], v[108:109]
	v_pk_add_f32 v[106:107], v[138:139], v[106:107]
	v_pk_add_f32 v[104:105], v[136:137], v[104:105]
	v_pk_add_f32 v[102:103], v[134:135], v[102:103]
	v_pk_add_f32 v[100:101], v[132:133], v[100:101]
	v_pk_add_f32 v[98:99], v[130:131], v[98:99]
	v_pk_add_f32 v[96:97], v[128:129], v[96:97]
	v_pk_add_f32 v[94:95], v[142:143], v[94:95]
	v_pk_add_f32 v[92:93], v[140:141], v[92:93]
	v_pk_add_f32 v[90:91], v[138:139], v[90:91]
	v_pk_add_f32 v[88:89], v[136:137], v[88:89]
	v_pk_add_f32 v[86:87], v[134:135], v[86:87]
	v_pk_add_f32 v[84:85], v[132:133], v[84:85]
	v_pk_add_f32 v[82:83], v[130:131], v[82:83]
	v_pk_add_f32 v[80:81], v[128:129], v[80:81]
	v_pk_add_f32 v[78:79], v[142:143], v[78:79]
	v_pk_add_f32 v[76:77], v[140:141], v[76:77]
	v_pk_add_f32 v[74:75], v[138:139], v[74:75]
	v_pk_add_f32 v[72:73], v[136:137], v[72:73]
	v_pk_add_f32 v[70:71], v[134:135], v[70:71]
	v_pk_add_f32 v[68:69], v[132:133], v[68:69]
	v_pk_add_f32 v[66:67], v[130:131], v[66:67]
	v_pk_add_f32 v[64:65], v[128:129], v[64:65]
	v_pk_add_f32 v[62:63], v[142:143], v[62:63]
	v_pk_add_f32 v[60:61], v[140:141], v[60:61]
	v_pk_add_f32 v[58:59], v[138:139], v[58:59]
	v_pk_add_f32 v[56:57], v[136:137], v[56:57]
	v_pk_add_f32 v[54:55], v[134:135], v[54:55]
	v_pk_add_f32 v[52:53], v[132:133], v[52:53]
	global_store_dwordx4 v[156:157], v[116:119], off nt
	global_store_dwordx4 v[156:157], v[124:127], off offset:64 nt
	global_store_dwordx4 v[156:157], v[120:123], off offset:512 nt
	global_store_dwordx4 v[156:157], v[112:115], off offset:576 nt
	global_store_dwordx4 v[172:173], v[108:111], off nt
	global_store_dwordx4 v[172:173], v[104:107], off offset:64 nt
	global_store_dwordx4 v[172:173], v[100:103], off offset:512 nt
	global_store_dwordx4 v[172:173], v[96:99], off offset:576 nt
	global_store_dwordx4 v[174:175], v[92:95], off nt
	global_store_dwordx4 v[174:175], v[88:91], off offset:64 nt
	global_store_dwordx4 v[174:175], v[84:87], off offset:512 nt
	global_store_dwordx4 v[174:175], v[80:83], off offset:576 nt
	global_store_dwordx4 v[176:177], v[76:79], off nt
	global_store_dwordx4 v[176:177], v[72:75], off offset:64 nt
	global_store_dwordx4 v[176:177], v[68:71], off offset:512 nt
	global_store_dwordx4 v[176:177], v[64:67], off offset:576 nt
	global_store_dwordx4 v[178:179], v[60:63], off nt
	global_store_dwordx4 v[178:179], v[56:59], off offset:64 nt
	global_store_dwordx4 v[178:179], v[52:55], off offset:512 nt
	global_store_dwordx4 v[178:179], v[48:51], off offset:576 nt
	v_pk_add_f32 v[34:35], v[130:131], v[34:35]
	v_pk_add_f32 v[32:33], v[128:129], v[32:33]
	v_add_u32_e32 v48, 0x90, v180
	v_mad_i64_i32 v[48:49], s[30:31], v48, s42, 0
	v_lshl_add_u64 v[48:49], v[48:49], 2, v[154:155]
	global_store_dwordx4 v[48:49], v[32:35], off offset:576 nt
	v_pk_add_f32 v[46:47], v[142:143], v[46:47]
	v_pk_add_f32 v[44:45], v[140:141], v[44:45]
	v_add_u32_e32 v32, 0xa0, v180
	v_mad_i64_i32 v[32:33], s[30:31], v32, s42, 0
	v_pk_add_f32 v[42:43], v[138:139], v[42:43]
	v_pk_add_f32 v[40:41], v[136:137], v[40:41]
	v_pk_add_f32 v[38:39], v[134:135], v[38:39]
	v_pk_add_f32 v[36:37], v[132:133], v[36:37]
	v_lshl_add_u64 v[32:33], v[32:33], 2, v[154:155]
	v_pk_add_f32 v[18:19], v[130:131], v[18:19]
	v_pk_add_f32 v[16:17], v[128:129], v[16:17]
	global_store_dwordx4 v[48:49], v[44:47], off nt
	global_store_dwordx4 v[48:49], v[40:43], off offset:64 nt
	global_store_dwordx4 v[48:49], v[36:39], off offset:512 nt
	global_store_dwordx4 v[32:33], v[16:19], off offset:576 nt
	v_pk_add_f32 v[30:31], v[142:143], v[30:31]
	v_pk_add_f32 v[28:29], v[140:141], v[28:29]
	v_add_u32_e32 v16, 0xb0, v180
	v_mad_i64_i32 v[16:17], s[30:31], v16, s42, 0
	v_pk_add_f32 v[26:27], v[138:139], v[26:27]
	v_pk_add_f32 v[24:25], v[136:137], v[24:25]
	v_pk_add_f32 v[22:23], v[134:135], v[22:23]
	v_pk_add_f32 v[20:21], v[132:133], v[20:21]
	v_lshl_add_u64 v[16:17], v[16:17], 2, v[154:155]
	v_pk_add_f32 v[14:15], v[142:143], v[14:15]
	v_pk_add_f32 v[12:13], v[140:141], v[12:13]
	v_pk_add_f32 v[10:11], v[138:139], v[10:11]
	v_pk_add_f32 v[8:9], v[136:137], v[8:9]
	v_pk_add_f32 v[6:7], v[134:135], v[6:7]
	v_pk_add_f32 v[4:5], v[132:133], v[4:5]
	v_pk_add_f32 v[2:3], v[130:131], v[2:3]
	v_pk_add_f32 v[0:1], v[128:129], v[0:1]
	s_mov_b64 s[30:31], s[4:5]
	global_store_dwordx4 v[32:33], v[28:31], off nt
	global_store_dwordx4 v[32:33], v[24:27], off offset:64 nt
	global_store_dwordx4 v[32:33], v[20:23], off offset:512 nt
	global_store_dwordx4 v[16:17], v[12:15], off nt
	global_store_dwordx4 v[16:17], v[8:11], off offset:64 nt
	global_store_dwordx4 v[16:17], v[4:7], off offset:512 nt
	global_store_dwordx4 v[16:17], v[0:3], off offset:576 nt
	s_cmpk_gt_u32 s41, 0xff
	s_cbranch_scc0 .Lus_g1_b
	s_barrier

.LBB3_31:
	s_add_i32 s4, s39, -1
	s_ashr_i32 s5, s4, 31
	s_lshl_b64 s[6:7], s[4:5], 7
	s_add_u32 s0, s0, s6
	s_addc_u32 s1, s1, s7
	s_lshl_b32 s4, s4, 15
	s_and_b32 s4, s4, 0x18000
	s_add_i32 s4, s4, 0
	s_add_i32 s4, s4, s40
	v_lshl_add_u64 v[80:81], s[0:1], 0, v[144:145]
	s_mov_b32 m0, s4
	s_waitcnt vmcnt(4)
	s_barrier
	global_load_lds_dwordx4 v[80:81], off
	s_add_i32 m0, s4, 0x2000
	v_lshl_add_u64 v[80:81], s[0:1], 0, v[146:147]
	s_add_u32 s0, s2, s6
	s_addc_u32 s1, s3, s7
	global_load_lds_dwordx4 v[80:81], off
	s_add_i32 m0, s4, 0x4000
	v_lshl_add_u64 v[80:81], s[0:1], 0, v[144:145]
	global_load_lds_dwordx4 v[80:81], off
	s_add_i32 m0, s4, 0x6000
	v_lshl_add_u64 v[80:81], s[0:1], 0, v[146:147]
	global_load_lds_dwordx4 v[80:81], off
	s_waitcnt lgkmcnt(0)
	s_lshl_b32 s0, s39, 15
	s_add_i32 s1, s0, 0x8000
	s_and_b32 s1, s1, 0x18000
	s_add_i32 s1, s1, 0
	v_add_u32_e32 v108, s1, v160
	ds_read_b128 v[80:83], v108
	ds_read_b128 v[84:87], v108 offset:1024
	ds_read_b128 v[88:91], v108 offset:2048
	ds_read_b128 v[92:95], v108 offset:3072
	ds_read_b128 v[96:99], v108 offset:4096
	ds_read_b128 v[100:103], v108 offset:5120
	ds_read_b128 v[104:107], v108 offset:6144
	ds_read_b128 v[108:111], v108 offset:7168
	v_add_u32_e32 v124, s1, v161
	ds_read_b128 v[112:115], v124 offset:16384
	ds_read_b128 v[116:119], v124 offset:17408
	ds_read_b128 v[120:123], v124 offset:18432
	ds_read_b128 v[124:127], v124 offset:19456
	v_mfma_f32_16x16x32_f16 v[76:79], v[36:39], v[44:47], v[76:79]
	v_mfma_f32_16x16x32_f16 v[44:47], v[28:31], v[44:47], v[72:75]
	v_mfma_f32_16x16x32_f16 v[76:79], v[32:35], v[40:43], v[76:79]
	v_mfma_f32_16x16x32_f16 v[40:43], v[24:27], v[40:43], v[44:47]
	v_mfma_f32_16x16x32_f16 v[44:47], v[36:39], v[20:23], v[68:71]
	v_mfma_f32_16x16x32_f16 v[20:23], v[28:31], v[20:23], v[64:67]
	v_mfma_f32_16x16x32_f16 v[44:47], v[32:35], v[16:19], v[44:47]
	v_mfma_f32_16x16x32_f16 v[16:19], v[24:27], v[16:19], v[20:23]
	v_mfma_f32_16x16x32_f16 v[20:23], v[36:39], v[12:15], v[60:63]
	v_mfma_f32_16x16x32_f16 v[12:15], v[28:31], v[12:15], v[56:59]
	v_mfma_f32_16x16x32_f16 v[20:23], v[32:35], v[8:11], v[20:23]
	v_mfma_f32_16x16x32_f16 v[8:11], v[24:27], v[8:11], v[12:15]
	v_mfma_f32_16x16x32_f16 v[12:15], v[36:39], v[4:7], v[52:55]
	v_mfma_f32_16x16x32_f16 v[4:7], v[28:31], v[4:7], v[48:51]
	v_mfma_f32_16x16x32_f16 v[12:15], v[32:35], v[0:3], v[12:15]
	v_mfma_f32_16x16x32_f16 v[0:3], v[24:27], v[0:3], v[4:7]
	s_waitcnt vmcnt(4)
	s_barrier
	s_waitcnt lgkmcnt(0)
	s_and_b32 s1, s0, 0x18000
	s_xor_b32 s1, s1, 0x10000
	s_add_i32 s1, s1, 0
	v_add_u32_e32 v56, s1, v160
	ds_read_b128 v[4:7], v56
	ds_read_b128 v[24:27], v56 offset:1024
	ds_read_b128 v[28:31], v56 offset:2048
	ds_read_b128 v[32:35], v56 offset:3072
	ds_read_b128 v[36:39], v56 offset:4096
	ds_read_b128 v[48:51], v56 offset:5120
	ds_read_b128 v[52:55], v56 offset:6144
	ds_read_b128 v[56:59], v56 offset:7168
	v_add_u32_e32 v72, s1, v161
	ds_read_b128 v[60:63], v72 offset:16384
	ds_read_b128 v[64:67], v72 offset:17408
	ds_read_b128 v[68:71], v72 offset:18432
	ds_read_b128 v[72:75], v72 offset:19456
	v_mfma_f32_16x16x32_f16 v[76:79], v[112:115], v[80:83], v[76:79]
	v_mfma_f32_16x16x32_f16 v[40:43], v[120:123], v[80:83], v[40:43]
	v_mfma_f32_16x16x32_f16 v[44:47], v[112:115], v[88:91], v[44:47]
	v_mfma_f32_16x16x32_f16 v[16:19], v[120:123], v[88:91], v[16:19]
	v_mfma_f32_16x16x32_f16 v[20:23], v[112:115], v[96:99], v[20:23]
	v_mfma_f32_16x16x32_f16 v[8:11], v[120:123], v[96:99], v[8:11]
	v_mfma_f32_16x16x32_f16 v[12:15], v[112:115], v[104:107], v[12:15]
	v_mfma_f32_16x16x32_f16 v[0:3], v[120:123], v[104:107], v[0:3]
	v_mfma_f32_16x16x32_f16 v[76:79], v[116:119], v[84:87], v[76:79]
	v_mfma_f32_16x16x32_f16 v[40:43], v[124:127], v[84:87], v[40:43]
	v_mfma_f32_16x16x32_f16 v[44:47], v[116:119], v[92:95], v[44:47]
	v_mfma_f32_16x16x32_f16 v[16:19], v[124:127], v[92:95], v[16:19]
	v_mfma_f32_16x16x32_f16 v[20:23], v[116:119], v[100:103], v[20:23]
	v_mfma_f32_16x16x32_f16 v[8:11], v[124:127], v[100:103], v[8:11]
	v_mfma_f32_16x16x32_f16 v[12:15], v[116:119], v[108:111], v[12:15]
	v_mfma_f32_16x16x32_f16 v[0:3], v[124:127], v[108:111], v[0:3]
	s_waitcnt vmcnt(0)
	s_barrier
	s_waitcnt lgkmcnt(0)
	s_add_i32 s0, s0, 0x18000
	s_and_b32 s0, s0, 0x18000
	s_add_i32 s0, s0, 0
	v_add_u32_e32 v108, s0, v160
	ds_read_b128 v[80:83], v108
	ds_read_b128 v[84:87], v108 offset:1024
	ds_read_b128 v[88:91], v108 offset:2048
	ds_read_b128 v[92:95], v108 offset:3072
	ds_read_b128 v[96:99], v108 offset:4096
	ds_read_b128 v[100:103], v108 offset:5120
	ds_read_b128 v[104:107], v108 offset:6144
	ds_read_b128 v[108:111], v108 offset:7168
	v_add_u32_e32 v124, s0, v161
	ds_read_b128 v[112:115], v124 offset:16384
	ds_read_b128 v[116:119], v124 offset:17408
	ds_read_b128 v[120:123], v124 offset:18432
	ds_read_b128 v[124:127], v124 offset:19456
	v_mfma_f32_16x16x32_f16 v[76:79], v[60:63], v[4:7], v[76:79]
	v_mfma_f32_16x16x32_f16 v[4:7], v[68:71], v[4:7], v[40:43]
	v_mfma_f32_16x16x32_f16 v[76:79], v[64:67], v[24:27], v[76:79]
	v_mfma_f32_16x16x32_f16 v[4:7], v[72:75], v[24:27], v[4:7]
	v_mfma_f32_16x16x32_f16 v[24:27], v[60:63], v[28:31], v[44:47]
	v_mfma_f32_16x16x32_f16 v[16:19], v[68:71], v[28:31], v[16:19]
	v_mfma_f32_16x16x32_f16 v[20:23], v[60:63], v[36:39], v[20:23]
	v_mfma_f32_16x16x32_f16 v[8:11], v[68:71], v[36:39], v[8:11]
	v_mfma_f32_16x16x32_f16 v[12:15], v[60:63], v[52:55], v[12:15]
	v_mfma_f32_16x16x32_f16 v[0:3], v[68:71], v[52:55], v[0:3]
	v_mfma_f32_16x16x32_f16 v[24:27], v[64:67], v[32:35], v[24:27]
	v_mfma_f32_16x16x32_f16 v[16:19], v[72:75], v[32:35], v[16:19]
	v_mfma_f32_16x16x32_f16 v[20:23], v[64:67], v[48:51], v[20:23]
	v_mfma_f32_16x16x32_f16 v[8:11], v[72:75], v[48:51], v[8:11]
	v_mfma_f32_16x16x32_f16 v[12:15], v[64:67], v[56:59], v[12:15]
	v_mfma_f32_16x16x32_f16 v[0:3], v[72:75], v[56:59], v[0:3]
	v_lshl_or_b32 v32, v159, 2, s38
	v_or_b32_e32 v32, s20, v32
	v_ashrrev_i32_e32 v33, 31, v32
	v_lshlrev_b64 v[40:41], 2, v[32:33]
	v_lshl_add_u64 v[36:37], s[10:11], 0, v[40:41]
	global_load_dwordx4 v[32:35], v[36:37], off
	s_waitcnt lgkmcnt(0)
	v_mfma_f32_16x16x32_f16 v[28:31], v[112:115], v[80:83], v[76:79]
	global_load_dwordx4 v[36:39], v[36:37], off offset:64
	s_add_i32 s33, s33, s12
	v_or_b32_e32 v44, s33, v158
	v_mfma_f32_16x16x32_f16 v[4:7], v[120:123], v[80:83], v[4:7]
	v_mad_i64_i32 v[42:43], s[0:1], v44, s13, 0
	v_or_b32_e32 v45, 16, v44
	v_mfma_f32_16x16x32_f16 v[24:27], v[112:115], v[88:91], v[24:27]
	v_or_b32_e32 v46, 32, v44
	v_or_b32_e32 v48, 48, v44
	v_lshl_add_u64 v[40:41], s[8:9], 0, v[40:41]
	v_mfma_f32_16x16x32_f16 v[16:19], v[120:123], v[88:91], v[16:19]
	v_mad_i64_i32 v[44:45], s[0:1], v45, s13, 0
	v_mad_i64_i32 v[46:47], s[0:1], v46, s13, 0
	v_mfma_f32_16x16x32_f16 v[20:23], v[112:115], v[96:99], v[20:23]
	v_mad_i64_i32 v[48:49], s[0:1], v48, s13, 0
	v_lshl_add_u64 v[42:43], v[42:43], 2, v[40:41]
	v_mfma_f32_16x16x32_f16 v[8:11], v[120:123], v[96:99], v[8:11]
	v_lshl_add_u64 v[44:45], v[44:45], 2, v[40:41]
	v_lshl_add_u64 v[46:47], v[46:47], 2, v[40:41]
	v_lshl_add_u64 v[40:41], v[48:49], 2, v[40:41]
	v_mfma_f32_16x16x32_f16 v[12:15], v[112:115], v[104:107], v[12:15]
	v_mfma_f32_16x16x32_f16 v[0:3], v[120:123], v[104:107], v[0:3]
	v_mfma_f32_16x16x32_f16 v[28:31], v[116:119], v[84:87], v[28:31]
	v_mfma_f32_16x16x32_f16 v[4:7], v[124:127], v[84:87], v[4:7]
	v_mfma_f32_16x16x32_f16 v[24:27], v[116:119], v[92:95], v[24:27]
	s_waitcnt vmcnt(0)
	s_nop 4
	v_pk_add_f32 v[30:31], v[34:35], v[30:31]
	v_mfma_f32_16x16x32_f16 v[16:19], v[124:127], v[92:95], v[16:19]
	v_add_f32_e64 v28, v32, v28
	v_add_f32_e64 v29, v33, v29
	v_pk_add_f32 v[6:7], v[38:39], v[6:7]
	v_pk_add_f32 v[4:5], v[36:37], v[4:5]
	v_mfma_f32_16x16x32_f16 v[20:23], v[116:119], v[100:103], v[20:23]
	v_add_f32_e64 v26, v34, v26
	v_add_f32_e64 v27, v35, v27
	v_pk_add_f32 v[24:25], v[32:33], v[24:25]
	v_pk_add_f32 v[18:19], v[38:39], v[18:19]
	v_mfma_f32_16x16x32_f16 v[8:11], v[124:127], v[100:103], v[8:11]
	v_add_f32_e64 v16, v36, v16
	v_add_f32_e64 v17, v37, v17
	s_nop 0
	v_pk_add_f32 v[22:23], v[34:35], v[22:23]
	v_pk_add_f32 v[20:21], v[32:33], v[20:21]
	v_mfma_f32_16x16x32_f16 v[12:15], v[116:119], v[108:111], v[12:15]
	v_mfma_f32_16x16x32_f16 v[0:3], v[124:127], v[108:111], v[0:3]
	s_nop 0
	v_add_f32_e64 v10, v38, v10
	v_add_f32_e64 v11, v39, v11
	v_pk_add_f32 v[8:9], v[36:37], v[8:9]
	s_nop 2
	v_pk_add_f32 v[14:15], v[34:35], v[14:15]
	v_pk_add_f32 v[12:13], v[32:33], v[12:13]
	v_pk_add_f32 v[2:3], v[38:39], v[2:3]
	v_pk_add_f32 v[0:1], v[36:37], v[0:1]
	global_store_dwordx4 v[42:43], v[28:31], off nt
	global_store_dwordx4 v[42:43], v[4:7], off offset:64 nt
	global_store_dwordx4 v[44:45], v[24:27], off nt
	global_store_dwordx4 v[44:45], v[16:19], off offset:64 nt
	global_store_dwordx4 v[46:47], v[20:23], off nt
	global_store_dwordx4 v[46:47], v[8:11], off offset:64 nt
	global_store_dwordx4 v[40:41], v[12:15], off nt
	global_store_dwordx4 v[40:41], v[0:3], off offset:64 nt
	s_bitcmp1_b32 s82, 5
	s_cbranch_scc0 .Lg1_done
	s_cmp_eq_u32 s84, 0
	s_cbranch_scc0 .Lg1_done
	s_mov_b32 s84, 1
	s_waitcnt lgkmcnt(0)
	s_barrier
	s_mov_b64 exec, -1
	s_mov_b64 s[0:1], s[80:81]
	s_mov_b32 s2, s82
	v_mbcnt_lo_u32_b32 v0, -1, 0
	v_mbcnt_hi_u32_b32 v0, -1, v0
	v_add_u32_e32 v0, s83, v0
	s_branch .Lg1_restart
